# baseline (speedup 1.0000x reference)
_Z11gemm_kernelILi1ELi1EEvPKDF16_S1_iiPKfS3_S3_PDF16_S4_S4_Pf:
	s_load_dwordx4 s[4:7], s[0:1], 0x0
	s_load_dwordx2 s[8:9], s[0:1], 0x48
	s_load_dwordx2 s[10:11], s[0:1], 0x18
	v_readfirstlane_b32 s12, v0
	v_and_b32_e32 v1, 63, v0
	s_lshr_b32 s12, s12, 6
	s_lshr_b32 s13, s12, 1
	s_and_b32 s14, s12, 1
	s_and_b32 s15, s2, 7
	s_lshr_b32 s16, s2, 3
	s_lshr_b32 s17, s16, 4
	s_lshl_b32 s15, s15, 2
	s_add_i32 s15, s15, s17
	s_and_b32 s16, s16, 15
	v_lshrrev_b32_e32 v2, 3, v1
	v_and_b32_e32 v3, 7, v1
	v_lshrrev_b32_e32 v4, 1, v2
	v_xor_b32_e32 v3, v3, v4
	v_lshlrev_b32_e32 v3, 4, v3
	v_lshl_or_b32 v2, v2, 11, v3
	v_xor_b32_e32 v3, 64, v2
	v_add_u32_e32 v3, 0x4000, v3
	v_add_u32_e32 v4, 0x8000, v2
	v_add_u32_e32 v5, 0x8000, v3
	v_and_b32_e32 v14, 31, v1
	v_lshlrev_b32_e32 v14, 2, v14
	s_lshl_b32 s20, s12, 12
	s_lshl_b32 s21, s12, 11
	s_add_i32 s21, s21, 0xc000
	s_lshl_b32 s22, s16, 8
	s_lshl_b32 s23, s14, 7
	s_add_i32 s22, s22, s23
	s_waitcnt lgkmcnt(0)
	s_add_u32 s10, s10, s22
	s_addc_u32 s11, s11, 0
	global_load_dword v14, v14, s[10:11]
	s_lshl_b32 s23, s15, 18
	s_lshl_b32 s24, s12, 16
	s_add_i32 s23, s23, s24
	s_add_u32 s4, s4, s23
	s_addc_u32 s5, s5, 0
	s_lshl_b32 s23, s16, 17
	s_lshl_b32 s24, s12, 15
	s_add_i32 s23, s23, s24
	s_add_u32 s6, s6, s23
	s_addc_u32 s7, s7, 0
	s_lshl_b32 s23, s15, 19
	s_lshl_b32 s24, s13, 18
	s_add_i32 s23, s23, s24
	s_add_i32 s23, s23, s22
	s_add_u32 s8, s8, s23
	s_addc_u32 s9, s9, 0
	s_add_u32 m0, s20, 0x0
	s_nop 0
	global_load_lds_dwordx4 v2, s[4:5]
	s_add_u32 m0, s20, 0x400
	s_nop 0
	global_load_lds_dwordx4 v3, s[4:5]
	s_add_u32 m0, s20, 0x800
	s_nop 0
	global_load_lds_dwordx4 v4, s[4:5]
	s_add_u32 m0, s20, 0xc00
	s_nop 0
	global_load_lds_dwordx4 v5, s[4:5]
	s_add_u32 m0, s21, 0x0
	s_nop 0
	global_load_lds_dwordx4 v2, s[6:7]
	s_add_u32 m0, s21, 0x400
	s_nop 0
	global_load_lds_dwordx4 v3, s[6:7]
	s_add_u32 s4, s4, 0x80
	s_addc_u32 s5, s5, 0
	s_add_u32 s6, s6, 0x80
	s_addc_u32 s7, s7, 0
	s_add_u32 m0, s20, 0x4000
	s_nop 0
	global_load_lds_dwordx4 v2, s[4:5]
	s_add_u32 m0, s20, 0x4400
	s_nop 0
	global_load_lds_dwordx4 v3, s[4:5]
	s_add_u32 m0, s20, 0x4800
	s_nop 0
	global_load_lds_dwordx4 v4, s[4:5]
	s_add_u32 m0, s20, 0x4c00
	s_nop 0
	global_load_lds_dwordx4 v5, s[4:5]
	s_add_u32 m0, s21, 0x2000
	s_nop 0
	global_load_lds_dwordx4 v2, s[6:7]
	s_add_u32 m0, s21, 0x2400
	s_nop 0
	global_load_lds_dwordx4 v3, s[6:7]
	s_add_u32 s4, s4, 0x80
	s_addc_u32 s5, s5, 0
	s_add_u32 s6, s6, 0x80
	s_addc_u32 s7, s7, 0
	v_and_b32_e32 v48, 31, v1
	v_lshrrev_b32_e32 v15, 5, v1
	v_bfe_u32 v16, v1, 1, 3
	v_xor_b32_e32 v16, v16, v15
	v_lshlrev_b32_e32 v16, 4, v16
	v_lshl_or_b32 v16, v48, 7, v16
	s_lshl_b32 s18, s13, 13
	s_lshl_b32 s19, s14, 12
	s_add_i32 s19, s19, 0xc000
	v_add_u32_e32 v6, s18, v16
	v_add_u32_e32 v10, s19, v16
	v_xor_b32_e32 v7, 0x20, v6
	v_xor_b32_e32 v11, 0x20, v10
	v_xor_b32_e32 v8, 0x40, v6
	v_xor_b32_e32 v12, 0x40, v10
	v_xor_b32_e32 v9, 0x60, v6
	v_xor_b32_e32 v13, 0x60, v10
	v_lshlrev_b32_e32 v15, 14, v15
	v_lshl_or_b32 v15, v48, 2, v15
	v_accvgpr_write_b32 a0, 0
	v_accvgpr_write_b32 a1, 0
	v_accvgpr_write_b32 a2, 0
	v_accvgpr_write_b32 a3, 0
	v_accvgpr_write_b32 a4, 0
	v_accvgpr_write_b32 a5, 0
	v_accvgpr_write_b32 a6, 0
	v_accvgpr_write_b32 a7, 0
	v_accvgpr_write_b32 a8, 0
	v_accvgpr_write_b32 a9, 0
	v_accvgpr_write_b32 a10, 0
	v_accvgpr_write_b32 a11, 0
	v_accvgpr_write_b32 a12, 0
	v_accvgpr_write_b32 a13, 0
	v_accvgpr_write_b32 a14, 0
	v_accvgpr_write_b32 a15, 0
	v_accvgpr_write_b32 a16, 0
	v_accvgpr_write_b32 a17, 0
	v_accvgpr_write_b32 a18, 0
	v_accvgpr_write_b32 a19, 0
	v_accvgpr_write_b32 a20, 0
	v_accvgpr_write_b32 a21, 0
	v_accvgpr_write_b32 a22, 0
	v_accvgpr_write_b32 a23, 0
	v_accvgpr_write_b32 a24, 0
	v_accvgpr_write_b32 a25, 0
	v_accvgpr_write_b32 a26, 0
	v_accvgpr_write_b32 a27, 0
	v_accvgpr_write_b32 a28, 0
	v_accvgpr_write_b32 a29, 0
	v_accvgpr_write_b32 a30, 0
	v_accvgpr_write_b32 a31, 0
	s_waitcnt vmcnt(6)
	s_barrier
	s_setprio 0
	ds_read_b128 v[16:19], v6 offset:0
	ds_read_b128 v[20:23], v6 offset:4096
	ds_read_b128 v[24:27], v10 offset:0
	s_add_u32 m0, s20, 0x8000
	ds_read_b128 v[28:31], v7 offset:0
	global_load_lds_dwordx4 v2, s[4:5]
	s_add_u32 m0, s20, 0x8400
	ds_read_b128 v[32:35], v7 offset:4096
	global_load_lds_dwordx4 v3, s[4:5]
	s_add_u32 m0, s20, 0x8800
	ds_read_b128 v[36:39], v11 offset:0
	global_load_lds_dwordx4 v4, s[4:5]
	s_add_u32 m0, s20, 0x8c00
	ds_read_b128 v[40:43], v8 offset:0
	global_load_lds_dwordx4 v5, s[4:5]
	s_add_u32 m0, s21, 0x4000
	ds_read_b128 v[44:47], v8 offset:4096
	global_load_lds_dwordx4 v2, s[6:7]
	s_add_u32 m0, s21, 0x4400
	ds_read_b128 v[48:51], v12 offset:0
	global_load_lds_dwordx4 v3, s[6:7]
	ds_read_b128 v[52:55], v9 offset:0
	ds_read_b128 v[56:59], v9 offset:4096
	ds_read_b128 v[60:63], v13 offset:0
	s_add_u32 s4, s4, 0x80
	s_addc_u32 s5, s5, 0
	s_add_u32 s6, s6, 0x80
	s_addc_u32 s7, s7, 0
	s_setprio 1
	s_waitcnt lgkmcnt(9)
	v_mfma_f32_32x32x16_f16 a[0:15], v[16:19], v[24:27], a[0:15]
	v_mfma_f32_32x32x16_f16 a[16:31], v[20:23], v[24:27], a[16:31]
	s_waitcnt lgkmcnt(6)
	v_mfma_f32_32x32x16_f16 a[0:15], v[28:31], v[36:39], a[0:15]
	v_mfma_f32_32x32x16_f16 a[16:31], v[32:35], v[36:39], a[16:31]
	s_waitcnt lgkmcnt(3)
	v_mfma_f32_32x32x16_f16 a[0:15], v[40:43], v[48:51], a[0:15]
	v_mfma_f32_32x32x16_f16 a[16:31], v[44:47], v[48:51], a[16:31]
	s_waitcnt lgkmcnt(0)
	v_mfma_f32_32x32x16_f16 a[0:15], v[52:55], v[60:63], a[0:15]
	v_mfma_f32_32x32x16_f16 a[16:31], v[56:59], v[60:63], a[16:31]
	s_waitcnt vmcnt(6)
	s_barrier
	s_setprio 0
	ds_read_b128 v[16:19], v6 offset:16384
	ds_read_b128 v[20:23], v6 offset:20480
	ds_read_b128 v[24:27], v10 offset:8192
	s_add_u32 m0, s20, 0x0
	ds_read_b128 v[28:31], v7 offset:16384
	global_load_lds_dwordx4 v2, s[4:5]
	s_add_u32 m0, s20, 0x400
	ds_read_b128 v[32:35], v7 offset:20480
	global_load_lds_dwordx4 v3, s[4:5]
	s_add_u32 m0, s20, 0x800
	ds_read_b128 v[36:39], v11 offset:8192
	global_load_lds_dwordx4 v4, s[4:5]
	s_add_u32 m0, s20, 0xc00
	ds_read_b128 v[40:43], v8 offset:16384
	global_load_lds_dwordx4 v5, s[4:5]
	s_add_u32 m0, s21, 0x0
	ds_read_b128 v[44:47], v8 offset:20480
	global_load_lds_dwordx4 v2, s[6:7]
	s_add_u32 m0, s21, 0x400
	ds_read_b128 v[48:51], v12 offset:8192
	global_load_lds_dwordx4 v3, s[6:7]
	ds_read_b128 v[52:55], v9 offset:16384
	ds_read_b128 v[56:59], v9 offset:20480
	ds_read_b128 v[60:63], v13 offset:8192
	s_add_u32 s4, s4, 0x80
	s_addc_u32 s5, s5, 0
	s_add_u32 s6, s6, 0x80
	s_addc_u32 s7, s7, 0
	s_setprio 1
	s_waitcnt lgkmcnt(9)
	v_mfma_f32_32x32x16_f16 a[0:15], v[16:19], v[24:27], a[0:15]
	v_mfma_f32_32x32x16_f16 a[16:31], v[20:23], v[24:27], a[16:31]
	s_waitcnt lgkmcnt(6)
	v_mfma_f32_32x32x16_f16 a[0:15], v[28:31], v[36:39], a[0:15]
	v_mfma_f32_32x32x16_f16 a[16:31], v[32:35], v[36:39], a[16:31]
	s_waitcnt lgkmcnt(3)
	v_mfma_f32_32x32x16_f16 a[0:15], v[40:43], v[48:51], a[0:15]
	v_mfma_f32_32x32x16_f16 a[16:31], v[44:47], v[48:51], a[16:31]
	s_waitcnt lgkmcnt(0)
	v_mfma_f32_32x32x16_f16 a[0:15], v[52:55], v[60:63], a[0:15]
	v_mfma_f32_32x32x16_f16 a[16:31], v[56:59], v[60:63], a[16:31]
	s_waitcnt vmcnt(6)
	s_barrier
	s_setprio 0
	ds_read_b128 v[16:19], v6 offset:32768
	ds_read_b128 v[20:23], v6 offset:36864
	ds_read_b128 v[24:27], v10 offset:16384
	s_add_u32 m0, s20, 0x4000
	ds_read_b128 v[28:31], v7 offset:32768
	global_load_lds_dwordx4 v2, s[4:5]
	s_add_u32 m0, s20, 0x4400
	ds_read_b128 v[32:35], v7 offset:36864
	global_load_lds_dwordx4 v3, s[4:5]
	s_add_u32 m0, s20, 0x4800
	ds_read_b128 v[36:39], v11 offset:16384
	global_load_lds_dwordx4 v4, s[4:5]
	s_add_u32 m0, s20, 0x4c00
	ds_read_b128 v[40:43], v8 offset:32768
	global_load_lds_dwordx4 v5, s[4:5]
	s_add_u32 m0, s21, 0x2000
	ds_read_b128 v[44:47], v8 offset:36864
	global_load_lds_dwordx4 v2, s[6:7]
	s_add_u32 m0, s21, 0x2400
	ds_read_b128 v[48:51], v12 offset:16384
	global_load_lds_dwordx4 v3, s[6:7]
	ds_read_b128 v[52:55], v9 offset:32768
	ds_read_b128 v[56:59], v9 offset:36864
	ds_read_b128 v[60:63], v13 offset:16384
	s_add_u32 s4, s4, 0x80
	s_addc_u32 s5, s5, 0
	s_add_u32 s6, s6, 0x80
	s_addc_u32 s7, s7, 0
	s_setprio 1
	s_waitcnt lgkmcnt(9)
	v_mfma_f32_32x32x16_f16 a[0:15], v[16:19], v[24:27], a[0:15]
	v_mfma_f32_32x32x16_f16 a[16:31], v[20:23], v[24:27], a[16:31]
	s_waitcnt lgkmcnt(6)
	v_mfma_f32_32x32x16_f16 a[0:15], v[28:31], v[36:39], a[0:15]
	v_mfma_f32_32x32x16_f16 a[16:31], v[32:35], v[36:39], a[16:31]
	s_waitcnt lgkmcnt(3)
	v_mfma_f32_32x32x16_f16 a[0:15], v[40:43], v[48:51], a[0:15]
	v_mfma_f32_32x32x16_f16 a[16:31], v[44:47], v[48:51], a[16:31]
	s_waitcnt lgkmcnt(0)
	v_mfma_f32_32x32x16_f16 a[0:15], v[52:55], v[60:63], a[0:15]
	v_mfma_f32_32x32x16_f16 a[16:31], v[56:59], v[60:63], a[16:31]
	s_waitcnt vmcnt(6)
	s_barrier
	s_setprio 0
	ds_read_b128 v[16:19], v6 offset:0
	ds_read_b128 v[20:23], v6 offset:4096
	ds_read_b128 v[24:27], v10 offset:0
	s_add_u32 m0, s20, 0x8000
	ds_read_b128 v[28:31], v7 offset:0
	global_load_lds_dwordx4 v2, s[4:5]
	s_add_u32 m0, s20, 0x8400
	ds_read_b128 v[32:35], v7 offset:4096
	global_load_lds_dwordx4 v3, s[4:5]
	s_add_u32 m0, s20, 0x8800
	ds_read_b128 v[36:39], v11 offset:0
	global_load_lds_dwordx4 v4, s[4:5]
	s_add_u32 m0, s20, 0x8c00
	ds_read_b128 v[40:43], v8 offset:0
	global_load_lds_dwordx4 v5, s[4:5]
	s_add_u32 m0, s21, 0x4000
	ds_read_b128 v[44:47], v8 offset:4096
	global_load_lds_dwordx4 v2, s[6:7]
	s_add_u32 m0, s21, 0x4400
	ds_read_b128 v[48:51], v12 offset:0
	global_load_lds_dwordx4 v3, s[6:7]
	ds_read_b128 v[52:55], v9 offset:0
	ds_read_b128 v[56:59], v9 offset:4096
	ds_read_b128 v[60:63], v13 offset:0
	s_add_u32 s4, s4, 0x80
	s_addc_u32 s5, s5, 0
	s_add_u32 s6, s6, 0x80
	s_addc_u32 s7, s7, 0
	s_setprio 1
	s_waitcnt lgkmcnt(9)
	v_mfma_f32_32x32x16_f16 a[0:15], v[16:19], v[24:27], a[0:15]
	v_mfma_f32_32x32x16_f16 a[16:31], v[20:23], v[24:27], a[16:31]
	s_waitcnt lgkmcnt(6)
	v_mfma_f32_32x32x16_f16 a[0:15], v[28:31], v[36:39], a[0:15]
	v_mfma_f32_32x32x16_f16 a[16:31], v[32:35], v[36:39], a[16:31]
	s_waitcnt lgkmcnt(3)
	v_mfma_f32_32x32x16_f16 a[0:15], v[40:43], v[48:51], a[0:15]
	v_mfma_f32_32x32x16_f16 a[16:31], v[44:47], v[48:51], a[16:31]
	s_waitcnt lgkmcnt(0)
	v_mfma_f32_32x32x16_f16 a[0:15], v[52:55], v[60:63], a[0:15]
	v_mfma_f32_32x32x16_f16 a[16:31], v[56:59], v[60:63], a[16:31]
	s_waitcnt vmcnt(6)
	s_barrier
	s_setprio 0
	ds_read_b128 v[16:19], v6 offset:16384
	ds_read_b128 v[20:23], v6 offset:20480
	ds_read_b128 v[24:27], v10 offset:8192
	s_add_u32 m0, s20, 0x0
	ds_read_b128 v[28:31], v7 offset:16384
	global_load_lds_dwordx4 v2, s[4:5]
	s_add_u32 m0, s20, 0x400
	ds_read_b128 v[32:35], v7 offset:20480
	global_load_lds_dwordx4 v3, s[4:5]
	s_add_u32 m0, s20, 0x800
	ds_read_b128 v[36:39], v11 offset:8192
	global_load_lds_dwordx4 v4, s[4:5]
	s_add_u32 m0, s20, 0xc00
	ds_read_b128 v[40:43], v8 offset:16384
	global_load_lds_dwordx4 v5, s[4:5]
	s_add_u32 m0, s21, 0x0
	ds_read_b128 v[44:47], v8 offset:20480
	global_load_lds_dwordx4 v2, s[6:7]
	s_add_u32 m0, s21, 0x400
	ds_read_b128 v[48:51], v12 offset:8192
	global_load_lds_dwordx4 v3, s[6:7]
	ds_read_b128 v[52:55], v9 offset:16384
	ds_read_b128 v[56:59], v9 offset:20480
	ds_read_b128 v[60:63], v13 offset:8192
	s_add_u32 s4, s4, 0x80
	s_addc_u32 s5, s5, 0
	s_add_u32 s6, s6, 0x80
	s_addc_u32 s7, s7, 0
	s_setprio 1
	s_waitcnt lgkmcnt(9)
	v_mfma_f32_32x32x16_f16 a[0:15], v[16:19], v[24:27], a[0:15]
	v_mfma_f32_32x32x16_f16 a[16:31], v[20:23], v[24:27], a[16:31]
	s_waitcnt lgkmcnt(6)
	v_mfma_f32_32x32x16_f16 a[0:15], v[28:31], v[36:39], a[0:15]
	v_mfma_f32_32x32x16_f16 a[16:31], v[32:35], v[36:39], a[16:31]
	s_waitcnt lgkmcnt(3)
	v_mfma_f32_32x32x16_f16 a[0:15], v[40:43], v[48:51], a[0:15]
	v_mfma_f32_32x32x16_f16 a[16:31], v[44:47], v[48:51], a[16:31]
	s_waitcnt lgkmcnt(0)
	v_mfma_f32_32x32x16_f16 a[0:15], v[52:55], v[60:63], a[0:15]
	v_mfma_f32_32x32x16_f16 a[16:31], v[56:59], v[60:63], a[16:31]
	s_waitcnt vmcnt(6)
	s_barrier
	s_setprio 0
	ds_read_b128 v[16:19], v6 offset:32768
	ds_read_b128 v[20:23], v6 offset:36864
	ds_read_b128 v[24:27], v10 offset:16384
	s_add_u32 m0, s20, 0x4000
	ds_read_b128 v[28:31], v7 offset:32768
	global_load_lds_dwordx4 v2, s[4:5]
	s_add_u32 m0, s20, 0x4400
	ds_read_b128 v[32:35], v7 offset:36864
	global_load_lds_dwordx4 v3, s[4:5]
	s_add_u32 m0, s20, 0x4800
	ds_read_b128 v[36:39], v11 offset:16384
	global_load_lds_dwordx4 v4, s[4:5]
	s_add_u32 m0, s20, 0x4c00
	ds_read_b128 v[40:43], v8 offset:32768
	global_load_lds_dwordx4 v5, s[4:5]
	s_add_u32 m0, s21, 0x2000
	ds_read_b128 v[44:47], v8 offset:36864
	global_load_lds_dwordx4 v2, s[6:7]
	s_add_u32 m0, s21, 0x2400
	ds_read_b128 v[48:51], v12 offset:16384
	global_load_lds_dwordx4 v3, s[6:7]
	ds_read_b128 v[52:55], v9 offset:32768
	ds_read_b128 v[56:59], v9 offset:36864
	ds_read_b128 v[60:63], v13 offset:16384
	s_add_u32 s4, s4, 0x80
	s_addc_u32 s5, s5, 0
	s_add_u32 s6, s6, 0x80
	s_addc_u32 s7, s7, 0
	s_setprio 1
	s_waitcnt lgkmcnt(9)
	v_mfma_f32_32x32x16_f16 a[0:15], v[16:19], v[24:27], a[0:15]
	v_mfma_f32_32x32x16_f16 a[16:31], v[20:23], v[24:27], a[16:31]
	s_waitcnt lgkmcnt(6)
	v_mfma_f32_32x32x16_f16 a[0:15], v[28:31], v[36:39], a[0:15]
	v_mfma_f32_32x32x16_f16 a[16:31], v[32:35], v[36:39], a[16:31]
	s_waitcnt lgkmcnt(3)
	v_mfma_f32_32x32x16_f16 a[0:15], v[40:43], v[48:51], a[0:15]
	v_mfma_f32_32x32x16_f16 a[16:31], v[44:47], v[48:51], a[16:31]
	s_waitcnt lgkmcnt(0)
	v_mfma_f32_32x32x16_f16 a[0:15], v[52:55], v[60:63], a[0:15]
	v_mfma_f32_32x32x16_f16 a[16:31], v[56:59], v[60:63], a[16:31]
	s_waitcnt vmcnt(6)
	s_barrier
	s_setprio 0
	ds_read_b128 v[16:19], v6 offset:0
	ds_read_b128 v[20:23], v6 offset:4096
	ds_read_b128 v[24:27], v10 offset:0
	s_add_u32 m0, s20, 0x8000
	ds_read_b128 v[28:31], v7 offset:0
	global_load_lds_dwordx4 v2, s[4:5]
	s_add_u32 m0, s20, 0x8400
	ds_read_b128 v[32:35], v7 offset:4096
	global_load_lds_dwordx4 v3, s[4:5]
	s_add_u32 m0, s20, 0x8800
	ds_read_b128 v[36:39], v11 offset:0
	global_load_lds_dwordx4 v4, s[4:5]
	s_add_u32 m0, s20, 0x8c00
	ds_read_b128 v[40:43], v8 offset:0
	global_load_lds_dwordx4 v5, s[4:5]
	s_add_u32 m0, s21, 0x4000
	ds_read_b128 v[44:47], v8 offset:4096
	global_load_lds_dwordx4 v2, s[6:7]
	s_add_u32 m0, s21, 0x4400
	ds_read_b128 v[48:51], v12 offset:0
	global_load_lds_dwordx4 v3, s[6:7]
	ds_read_b128 v[52:55], v9 offset:0
	ds_read_b128 v[56:59], v9 offset:4096
	ds_read_b128 v[60:63], v13 offset:0
	s_add_u32 s4, s4, 0x80
	s_addc_u32 s5, s5, 0
	s_add_u32 s6, s6, 0x80
	s_addc_u32 s7, s7, 0
	s_setprio 1
	s_waitcnt lgkmcnt(9)
	v_mfma_f32_32x32x16_f16 a[0:15], v[16:19], v[24:27], a[0:15]
	v_mfma_f32_32x32x16_f16 a[16:31], v[20:23], v[24:27], a[16:31]
	s_waitcnt lgkmcnt(6)
	v_mfma_f32_32x32x16_f16 a[0:15], v[28:31], v[36:39], a[0:15]
	v_mfma_f32_32x32x16_f16 a[16:31], v[32:35], v[36:39], a[16:31]
	s_waitcnt lgkmcnt(3)
	v_mfma_f32_32x32x16_f16 a[0:15], v[40:43], v[48:51], a[0:15]
	v_mfma_f32_32x32x16_f16 a[16:31], v[44:47], v[48:51], a[16:31]
	s_waitcnt lgkmcnt(0)
	v_mfma_f32_32x32x16_f16 a[0:15], v[52:55], v[60:63], a[0:15]
	v_mfma_f32_32x32x16_f16 a[16:31], v[56:59], v[60:63], a[16:31]
	s_waitcnt vmcnt(6)
	s_barrier
	s_setprio 0
	ds_read_b128 v[16:19], v6 offset:16384
	ds_read_b128 v[20:23], v6 offset:20480
	ds_read_b128 v[24:27], v10 offset:8192
	s_add_u32 m0, s20, 0x0
	ds_read_b128 v[28:31], v7 offset:16384
	global_load_lds_dwordx4 v2, s[4:5]
	s_add_u32 m0, s20, 0x400
	ds_read_b128 v[32:35], v7 offset:20480
	global_load_lds_dwordx4 v3, s[4:5]
	s_add_u32 m0, s20, 0x800
	ds_read_b128 v[36:39], v11 offset:8192
	global_load_lds_dwordx4 v4, s[4:5]
	s_add_u32 m0, s20, 0xc00
	ds_read_b128 v[40:43], v8 offset:16384
	global_load_lds_dwordx4 v5, s[4:5]
	s_add_u32 m0, s21, 0x0
	ds_read_b128 v[44:47], v8 offset:20480
	global_load_lds_dwordx4 v2, s[6:7]
	s_add_u32 m0, s21, 0x400
	ds_read_b128 v[48:51], v12 offset:8192
	global_load_lds_dwordx4 v3, s[6:7]
	ds_read_b128 v[52:55], v9 offset:16384
	ds_read_b128 v[56:59], v9 offset:20480
	ds_read_b128 v[60:63], v13 offset:8192
	s_add_u32 s4, s4, 0x80
	s_addc_u32 s5, s5, 0
	s_add_u32 s6, s6, 0x80
	s_addc_u32 s7, s7, 0
	s_setprio 1
	s_waitcnt lgkmcnt(9)
	v_mfma_f32_32x32x16_f16 a[0:15], v[16:19], v[24:27], a[0:15]
	v_mfma_f32_32x32x16_f16 a[16:31], v[20:23], v[24:27], a[16:31]
	s_waitcnt lgkmcnt(6)
	v_mfma_f32_32x32x16_f16 a[0:15], v[28:31], v[36:39], a[0:15]
	v_mfma_f32_32x32x16_f16 a[16:31], v[32:35], v[36:39], a[16:31]
	s_waitcnt lgkmcnt(3)
	v_mfma_f32_32x32x16_f16 a[0:15], v[40:43], v[48:51], a[0:15]
	v_mfma_f32_32x32x16_f16 a[16:31], v[44:47], v[48:51], a[16:31]
	s_waitcnt lgkmcnt(0)
	v_mfma_f32_32x32x16_f16 a[0:15], v[52:55], v[60:63], a[0:15]
	v_mfma_f32_32x32x16_f16 a[16:31], v[56:59], v[60:63], a[16:31]
	s_waitcnt vmcnt(6)
	s_barrier
	s_setprio 0
	ds_read_b128 v[16:19], v6 offset:32768
	ds_read_b128 v[20:23], v6 offset:36864
	ds_read_b128 v[24:27], v10 offset:16384
	s_add_u32 m0, s20, 0x4000
	ds_read_b128 v[28:31], v7 offset:32768
	global_load_lds_dwordx4 v2, s[4:5]
	s_add_u32 m0, s20, 0x4400
	ds_read_b128 v[32:35], v7 offset:36864
	global_load_lds_dwordx4 v3, s[4:5]
	s_add_u32 m0, s20, 0x4800
	ds_read_b128 v[36:39], v11 offset:16384
	global_load_lds_dwordx4 v4, s[4:5]
	s_add_u32 m0, s20, 0x4c00
	ds_read_b128 v[40:43], v8 offset:32768
	global_load_lds_dwordx4 v5, s[4:5]
	s_add_u32 m0, s21, 0x2000
	ds_read_b128 v[44:47], v8 offset:36864
	global_load_lds_dwordx4 v2, s[6:7]
	s_add_u32 m0, s21, 0x2400
	ds_read_b128 v[48:51], v12 offset:16384
	global_load_lds_dwordx4 v3, s[6:7]
	ds_read_b128 v[52:55], v9 offset:32768
	ds_read_b128 v[56:59], v9 offset:36864
	ds_read_b128 v[60:63], v13 offset:16384
	s_add_u32 s4, s4, 0x80
	s_addc_u32 s5, s5, 0
	s_add_u32 s6, s6, 0x80
	s_addc_u32 s7, s7, 0
	s_setprio 1
	s_waitcnt lgkmcnt(9)
	v_mfma_f32_32x32x16_f16 a[0:15], v[16:19], v[24:27], a[0:15]
	v_mfma_f32_32x32x16_f16 a[16:31], v[20:23], v[24:27], a[16:31]
	s_waitcnt lgkmcnt(6)
	v_mfma_f32_32x32x16_f16 a[0:15], v[28:31], v[36:39], a[0:15]
	v_mfma_f32_32x32x16_f16 a[16:31], v[32:35], v[36:39], a[16:31]
	s_waitcnt lgkmcnt(3)
	v_mfma_f32_32x32x16_f16 a[0:15], v[40:43], v[48:51], a[0:15]
	v_mfma_f32_32x32x16_f16 a[16:31], v[44:47], v[48:51], a[16:31]
	s_waitcnt lgkmcnt(0)
	v_mfma_f32_32x32x16_f16 a[0:15], v[52:55], v[60:63], a[0:15]
	v_mfma_f32_32x32x16_f16 a[16:31], v[56:59], v[60:63], a[16:31]
	s_waitcnt vmcnt(6)
	s_barrier
	s_setprio 0
	ds_read_b128 v[16:19], v6 offset:0
	ds_read_b128 v[20:23], v6 offset:4096
	ds_read_b128 v[24:27], v10 offset:0
	s_add_u32 m0, s20, 0x8000
	ds_read_b128 v[28:31], v7 offset:0
	global_load_lds_dwordx4 v2, s[4:5]
	s_add_u32 m0, s20, 0x8400
	ds_read_b128 v[32:35], v7 offset:4096
	global_load_lds_dwordx4 v3, s[4:5]
	s_add_u32 m0, s20, 0x8800
	ds_read_b128 v[36:39], v11 offset:0
	global_load_lds_dwordx4 v4, s[4:5]
	s_add_u32 m0, s20, 0x8c00
	ds_read_b128 v[40:43], v8 offset:0
	global_load_lds_dwordx4 v5, s[4:5]
	s_add_u32 m0, s21, 0x4000
	ds_read_b128 v[44:47], v8 offset:4096
	global_load_lds_dwordx4 v2, s[6:7]
	s_add_u32 m0, s21, 0x4400
	ds_read_b128 v[48:51], v12 offset:0
	global_load_lds_dwordx4 v3, s[6:7]
	ds_read_b128 v[52:55], v9 offset:0
	ds_read_b128 v[56:59], v9 offset:4096
	ds_read_b128 v[60:63], v13 offset:0
	s_add_u32 s4, s4, 0x80
	s_addc_u32 s5, s5, 0
	s_add_u32 s6, s6, 0x80
	s_addc_u32 s7, s7, 0
	s_setprio 1
	s_waitcnt lgkmcnt(9)
	v_mfma_f32_32x32x16_f16 a[0:15], v[16:19], v[24:27], a[0:15]
	v_mfma_f32_32x32x16_f16 a[16:31], v[20:23], v[24:27], a[16:31]
	s_waitcnt lgkmcnt(6)
	v_mfma_f32_32x32x16_f16 a[0:15], v[28:31], v[36:39], a[0:15]
	v_mfma_f32_32x32x16_f16 a[16:31], v[32:35], v[36:39], a[16:31]
	s_waitcnt lgkmcnt(3)
	v_mfma_f32_32x32x16_f16 a[0:15], v[40:43], v[48:51], a[0:15]
	v_mfma_f32_32x32x16_f16 a[16:31], v[44:47], v[48:51], a[16:31]
	s_waitcnt lgkmcnt(0)
	v_mfma_f32_32x32x16_f16 a[0:15], v[52:55], v[60:63], a[0:15]
	v_mfma_f32_32x32x16_f16 a[16:31], v[56:59], v[60:63], a[16:31]
	s_waitcnt vmcnt(6)
	s_barrier
	s_setprio 0
	ds_read_b128 v[16:19], v6 offset:16384
	ds_read_b128 v[20:23], v6 offset:20480
	ds_read_b128 v[24:27], v10 offset:8192
	s_add_u32 m0, s20, 0x0
	ds_read_b128 v[28:31], v7 offset:16384
	global_load_lds_dwordx4 v2, s[4:5]
	s_add_u32 m0, s20, 0x400
	ds_read_b128 v[32:35], v7 offset:20480
	global_load_lds_dwordx4 v3, s[4:5]
	s_add_u32 m0, s20, 0x800
	ds_read_b128 v[36:39], v11 offset:8192
	global_load_lds_dwordx4 v4, s[4:5]
	s_add_u32 m0, s20, 0xc00
	ds_read_b128 v[40:43], v8 offset:16384
	global_load_lds_dwordx4 v5, s[4:5]
	s_add_u32 m0, s21, 0x0
	ds_read_b128 v[44:47], v8 offset:20480
	global_load_lds_dwordx4 v2, s[6:7]
	s_add_u32 m0, s21, 0x400
	ds_read_b128 v[48:51], v12 offset:8192
	global_load_lds_dwordx4 v3, s[6:7]
	ds_read_b128 v[52:55], v9 offset:16384
	ds_read_b128 v[56:59], v9 offset:20480
	ds_read_b128 v[60:63], v13 offset:8192
	s_add_u32 s4, s4, 0x80
	s_addc_u32 s5, s5, 0
	s_add_u32 s6, s6, 0x80
	s_addc_u32 s7, s7, 0
	s_setprio 1
	s_waitcnt lgkmcnt(9)
	v_mfma_f32_32x32x16_f16 a[0:15], v[16:19], v[24:27], a[0:15]
	v_mfma_f32_32x32x16_f16 a[16:31], v[20:23], v[24:27], a[16:31]
	s_waitcnt lgkmcnt(6)
	v_mfma_f32_32x32x16_f16 a[0:15], v[28:31], v[36:39], a[0:15]
	v_mfma_f32_32x32x16_f16 a[16:31], v[32:35], v[36:39], a[16:31]
	s_waitcnt lgkmcnt(3)
	v_mfma_f32_32x32x16_f16 a[0:15], v[40:43], v[48:51], a[0:15]
	v_mfma_f32_32x32x16_f16 a[16:31], v[44:47], v[48:51], a[16:31]
	s_waitcnt lgkmcnt(0)
	v_mfma_f32_32x32x16_f16 a[0:15], v[52:55], v[60:63], a[0:15]
	v_mfma_f32_32x32x16_f16 a[16:31], v[56:59], v[60:63], a[16:31]
	s_waitcnt vmcnt(6)
	s_barrier
	s_setprio 0
	ds_read_b128 v[16:19], v6 offset:32768
	ds_read_b128 v[20:23], v6 offset:36864
	ds_read_b128 v[24:27], v10 offset:16384
	s_add_u32 m0, s20, 0x4000
	ds_read_b128 v[28:31], v7 offset:32768
	global_load_lds_dwordx4 v2, s[4:5]
	s_add_u32 m0, s20, 0x4400
	ds_read_b128 v[32:35], v7 offset:36864
	global_load_lds_dwordx4 v3, s[4:5]
	s_add_u32 m0, s20, 0x4800
	ds_read_b128 v[36:39], v11 offset:16384
	global_load_lds_dwordx4 v4, s[4:5]
	s_add_u32 m0, s20, 0x4c00
	ds_read_b128 v[40:43], v8 offset:32768
	global_load_lds_dwordx4 v5, s[4:5]
	s_add_u32 m0, s21, 0x2000
	ds_read_b128 v[44:47], v8 offset:36864
	global_load_lds_dwordx4 v2, s[6:7]
	s_add_u32 m0, s21, 0x2400
	ds_read_b128 v[48:51], v12 offset:16384
	global_load_lds_dwordx4 v3, s[6:7]
	ds_read_b128 v[52:55], v9 offset:32768
	ds_read_b128 v[56:59], v9 offset:36864
	ds_read_b128 v[60:63], v13 offset:16384
	s_add_u32 s4, s4, 0x80
	s_addc_u32 s5, s5, 0
	s_add_u32 s6, s6, 0x80
	s_addc_u32 s7, s7, 0
	s_setprio 1
	s_waitcnt lgkmcnt(9)
	v_mfma_f32_32x32x16_f16 a[0:15], v[16:19], v[24:27], a[0:15]
	v_mfma_f32_32x32x16_f16 a[16:31], v[20:23], v[24:27], a[16:31]
	s_waitcnt lgkmcnt(6)
	v_mfma_f32_32x32x16_f16 a[0:15], v[28:31], v[36:39], a[0:15]
	v_mfma_f32_32x32x16_f16 a[16:31], v[32:35], v[36:39], a[16:31]
	s_waitcnt lgkmcnt(3)
	v_mfma_f32_32x32x16_f16 a[0:15], v[40:43], v[48:51], a[0:15]
	v_mfma_f32_32x32x16_f16 a[16:31], v[44:47], v[48:51], a[16:31]
	s_waitcnt lgkmcnt(0)
	v_mfma_f32_32x32x16_f16 a[0:15], v[52:55], v[60:63], a[0:15]
	v_mfma_f32_32x32x16_f16 a[16:31], v[56:59], v[60:63], a[16:31]
	s_waitcnt vmcnt(6)
	s_barrier
	s_setprio 0
	ds_read_b128 v[16:19], v6 offset:0
	ds_read_b128 v[20:23], v6 offset:4096
	ds_read_b128 v[24:27], v10 offset:0
	s_add_u32 m0, s20, 0x8000
	ds_read_b128 v[28:31], v7 offset:0
	global_load_lds_dwordx4 v2, s[4:5]
	s_add_u32 m0, s20, 0x8400
	ds_read_b128 v[32:35], v7 offset:4096
	global_load_lds_dwordx4 v3, s[4:5]
	s_add_u32 m0, s20, 0x8800
	ds_read_b128 v[36:39], v11 offset:0
	global_load_lds_dwordx4 v4, s[4:5]
	s_add_u32 m0, s20, 0x8c00
	ds_read_b128 v[40:43], v8 offset:0
	global_load_lds_dwordx4 v5, s[4:5]
	s_add_u32 m0, s21, 0x4000
	ds_read_b128 v[44:47], v8 offset:4096
	global_load_lds_dwordx4 v2, s[6:7]
	s_add_u32 m0, s21, 0x4400
	ds_read_b128 v[48:51], v12 offset:0
	global_load_lds_dwordx4 v3, s[6:7]
	ds_read_b128 v[52:55], v9 offset:0
	ds_read_b128 v[56:59], v9 offset:4096
	ds_read_b128 v[60:63], v13 offset:0
	s_add_u32 s4, s4, 0x80
	s_addc_u32 s5, s5, 0
	s_add_u32 s6, s6, 0x80
	s_addc_u32 s7, s7, 0
	s_setprio 1
	s_waitcnt lgkmcnt(9)
	v_mfma_f32_32x32x16_f16 a[0:15], v[16:19], v[24:27], a[0:15]
	v_mfma_f32_32x32x16_f16 a[16:31], v[20:23], v[24:27], a[16:31]
	s_waitcnt lgkmcnt(6)
	v_mfma_f32_32x32x16_f16 a[0:15], v[28:31], v[36:39], a[0:15]
	v_mfma_f32_32x32x16_f16 a[16:31], v[32:35], v[36:39], a[16:31]
	s_waitcnt lgkmcnt(3)
	v_mfma_f32_32x32x16_f16 a[0:15], v[40:43], v[48:51], a[0:15]
	v_mfma_f32_32x32x16_f16 a[16:31], v[44:47], v[48:51], a[16:31]
	s_waitcnt lgkmcnt(0)
	v_mfma_f32_32x32x16_f16 a[0:15], v[52:55], v[60:63], a[0:15]
	v_mfma_f32_32x32x16_f16 a[16:31], v[56:59], v[60:63], a[16:31]
	s_waitcnt vmcnt(6)
	s_barrier
	s_setprio 0
	ds_read_b128 v[16:19], v6 offset:16384
	ds_read_b128 v[20:23], v6 offset:20480
	ds_read_b128 v[24:27], v10 offset:8192
	s_add_u32 m0, s20, 0x0
	ds_read_b128 v[28:31], v7 offset:16384
	global_load_lds_dwordx4 v2, s[4:5]
	s_add_u32 m0, s20, 0x400
	ds_read_b128 v[32:35], v7 offset:20480
	global_load_lds_dwordx4 v3, s[4:5]
	s_add_u32 m0, s20, 0x800
	ds_read_b128 v[36:39], v11 offset:8192
	global_load_lds_dwordx4 v4, s[4:5]
	s_add_u32 m0, s20, 0xc00
	ds_read_b128 v[40:43], v8 offset:16384
	global_load_lds_dwordx4 v5, s[4:5]
	s_add_u32 m0, s21, 0x0
	ds_read_b128 v[44:47], v8 offset:20480
	global_load_lds_dwordx4 v2, s[6:7]
	s_add_u32 m0, s21, 0x400
	ds_read_b128 v[48:51], v12 offset:8192
	global_load_lds_dwordx4 v3, s[6:7]
	ds_read_b128 v[52:55], v9 offset:16384
	ds_read_b128 v[56:59], v9 offset:20480
	ds_read_b128 v[60:63], v13 offset:8192
	s_add_u32 s4, s4, 0x80
	s_addc_u32 s5, s5, 0
	s_add_u32 s6, s6, 0x80
	s_addc_u32 s7, s7, 0
	s_setprio 1
	s_waitcnt lgkmcnt(9)
	v_mfma_f32_32x32x16_f16 a[0:15], v[16:19], v[24:27], a[0:15]
	v_mfma_f32_32x32x16_f16 a[16:31], v[20:23], v[24:27], a[16:31]
	s_waitcnt lgkmcnt(6)
	v_mfma_f32_32x32x16_f16 a[0:15], v[28:31], v[36:39], a[0:15]
	v_mfma_f32_32x32x16_f16 a[16:31], v[32:35], v[36:39], a[16:31]
	s_waitcnt lgkmcnt(3)
	v_mfma_f32_32x32x16_f16 a[0:15], v[40:43], v[48:51], a[0:15]
	v_mfma_f32_32x32x16_f16 a[16:31], v[44:47], v[48:51], a[16:31]
	s_waitcnt lgkmcnt(0)
	v_mfma_f32_32x32x16_f16 a[0:15], v[52:55], v[60:63], a[0:15]
	v_mfma_f32_32x32x16_f16 a[16:31], v[56:59], v[60:63], a[16:31]
	s_waitcnt vmcnt(6)
	s_barrier
	s_setprio 0
	ds_read_b128 v[16:19], v6 offset:32768
	ds_read_b128 v[20:23], v6 offset:36864
	ds_read_b128 v[24:27], v10 offset:16384
	ds_read_b128 v[28:31], v7 offset:32768
	ds_read_b128 v[32:35], v7 offset:36864
	ds_read_b128 v[36:39], v11 offset:16384
	ds_read_b128 v[40:43], v8 offset:32768
	ds_read_b128 v[44:47], v8 offset:36864
	ds_read_b128 v[48:51], v12 offset:16384
	ds_read_b128 v[52:55], v9 offset:32768
	ds_read_b128 v[56:59], v9 offset:36864
	ds_read_b128 v[60:63], v13 offset:16384
	s_setprio 1
	s_waitcnt lgkmcnt(9)
	v_mfma_f32_32x32x16_f16 a[0:15], v[16:19], v[24:27], a[0:15]
	v_mfma_f32_32x32x16_f16 a[16:31], v[20:23], v[24:27], a[16:31]
	s_waitcnt lgkmcnt(6)
	v_mfma_f32_32x32x16_f16 a[0:15], v[28:31], v[36:39], a[0:15]
	v_mfma_f32_32x32x16_f16 a[16:31], v[32:35], v[36:39], a[16:31]
	s_waitcnt lgkmcnt(3)
	v_mfma_f32_32x32x16_f16 a[0:15], v[40:43], v[48:51], a[0:15]
	v_mfma_f32_32x32x16_f16 a[16:31], v[44:47], v[48:51], a[16:31]
	s_waitcnt lgkmcnt(0)
	v_mfma_f32_32x32x16_f16 a[0:15], v[52:55], v[60:63], a[0:15]
	v_mfma_f32_32x32x16_f16 a[16:31], v[56:59], v[60:63], a[16:31]
	s_waitcnt vmcnt(0)
	s_barrier
	s_setprio 0
	ds_read_b128 v[16:19], v6 offset:0
	ds_read_b128 v[20:23], v6 offset:4096
	ds_read_b128 v[24:27], v10 offset:0
	ds_read_b128 v[28:31], v7 offset:0
	ds_read_b128 v[32:35], v7 offset:4096
	ds_read_b128 v[36:39], v11 offset:0
	ds_read_b128 v[40:43], v8 offset:0
	ds_read_b128 v[44:47], v8 offset:4096
	ds_read_b128 v[48:51], v12 offset:0
	ds_read_b128 v[52:55], v9 offset:0
	ds_read_b128 v[56:59], v9 offset:4096
	ds_read_b128 v[60:63], v13 offset:0
	s_setprio 1
	s_waitcnt lgkmcnt(9)
	v_mfma_f32_32x32x16_f16 a[0:15], v[16:19], v[24:27], a[0:15]
	v_mfma_f32_32x32x16_f16 a[16:31], v[20:23], v[24:27], a[16:31]
	s_waitcnt lgkmcnt(6)
	v_mfma_f32_32x32x16_f16 a[0:15], v[28:31], v[36:39], a[0:15]
	v_mfma_f32_32x32x16_f16 a[16:31], v[32:35], v[36:39], a[16:31]
	s_waitcnt lgkmcnt(3)
	v_mfma_f32_32x32x16_f16 a[0:15], v[40:43], v[48:51], a[0:15]
	v_mfma_f32_32x32x16_f16 a[16:31], v[44:47], v[48:51], a[16:31]
	s_waitcnt lgkmcnt(0)
	v_mfma_f32_32x32x16_f16 a[0:15], v[52:55], v[60:63], a[0:15]
	v_mfma_f32_32x32x16_f16 a[16:31], v[56:59], v[60:63], a[16:31]
	s_setprio 0
	s_nop 15
	s_nop 3
	v_accvgpr_read_b32 v16, a0
	v_accvgpr_read_b32 v17, a1
	v_accvgpr_read_b32 v18, a2
	v_accvgpr_read_b32 v19, a3
	v_accvgpr_read_b32 v20, a4
	v_accvgpr_read_b32 v21, a5
	v_accvgpr_read_b32 v22, a6
	v_accvgpr_read_b32 v23, a7
	v_accvgpr_read_b32 v24, a8
	v_accvgpr_read_b32 v25, a9
	v_accvgpr_read_b32 v26, a10
	v_accvgpr_read_b32 v27, a11
	v_accvgpr_read_b32 v28, a12
	v_accvgpr_read_b32 v29, a13
	v_accvgpr_read_b32 v30, a14
	v_accvgpr_read_b32 v31, a15
	v_accvgpr_read_b32 v32, a16
	v_accvgpr_read_b32 v33, a17
	v_accvgpr_read_b32 v34, a18
	v_accvgpr_read_b32 v35, a19
	v_accvgpr_read_b32 v36, a20
	v_accvgpr_read_b32 v37, a21
	v_accvgpr_read_b32 v38, a22
	v_accvgpr_read_b32 v39, a23
	v_accvgpr_read_b32 v40, a24
	v_accvgpr_read_b32 v41, a25
	v_accvgpr_read_b32 v42, a26
	v_accvgpr_read_b32 v43, a27
	v_accvgpr_read_b32 v44, a28
	v_accvgpr_read_b32 v45, a29
	v_accvgpr_read_b32 v46, a30
	v_accvgpr_read_b32 v47, a31
	v_add_f32_e32 v16, v14, v16
	v_add_f32_e32 v17, v14, v17
	v_add_f32_e32 v18, v14, v18
	v_add_f32_e32 v19, v14, v19
	v_add_f32_e32 v20, v14, v20
	v_add_f32_e32 v21, v14, v21
	v_add_f32_e32 v22, v14, v22
	v_add_f32_e32 v23, v14, v23
	v_add_f32_e32 v24, v14, v24
	v_add_f32_e32 v25, v14, v25
	v_add_f32_e32 v26, v14, v26
	v_add_f32_e32 v27, v14, v27
	v_add_f32_e32 v28, v14, v28
	v_add_f32_e32 v29, v14, v29
	v_add_f32_e32 v30, v14, v30
	v_add_f32_e32 v31, v14, v31
	v_add_f32_e32 v32, v14, v32
	v_add_f32_e32 v33, v14, v33
	v_add_f32_e32 v34, v14, v34
	v_add_f32_e32 v35, v14, v35
	v_add_f32_e32 v36, v14, v36
	v_add_f32_e32 v37, v14, v37
	v_add_f32_e32 v38, v14, v38
	v_add_f32_e32 v39, v14, v39
	v_add_f32_e32 v40, v14, v40
	v_add_f32_e32 v41, v14, v41
	v_add_f32_e32 v42, v14, v42
	v_add_f32_e32 v43, v14, v43
	v_add_f32_e32 v44, v14, v44
	v_add_f32_e32 v45, v14, v45
	v_add_f32_e32 v46, v14, v46
	v_add_f32_e32 v47, v14, v47
	global_store_dword v15, v16, s[8:9] nt
	s_add_u32 s8, s8, 0x1000
	s_addc_u32 s9, s9, 0
	global_store_dword v15, v17, s[8:9] nt
	s_add_u32 s8, s8, 0x1000
	s_addc_u32 s9, s9, 0
	global_store_dword v15, v18, s[8:9] nt
	s_add_u32 s8, s8, 0x1000
	s_addc_u32 s9, s9, 0
	global_store_dword v15, v19, s[8:9] nt
	s_add_u32 s8, s8, 0x5000
	s_addc_u32 s9, s9, 0
	global_store_dword v15, v20, s[8:9] nt
	s_add_u32 s8, s8, 0x1000
	s_addc_u32 s9, s9, 0
	global_store_dword v15, v21, s[8:9] nt
	s_add_u32 s8, s8, 0x1000
	s_addc_u32 s9, s9, 0
	global_store_dword v15, v22, s[8:9] nt
	s_add_u32 s8, s8, 0x1000
	s_addc_u32 s9, s9, 0
	global_store_dword v15, v23, s[8:9] nt
	s_add_u32 s8, s8, 0x5000
	s_addc_u32 s9, s9, 0
	global_store_dword v15, v24, s[8:9] nt
	s_add_u32 s8, s8, 0x1000
	s_addc_u32 s9, s9, 0
	global_store_dword v15, v25, s[8:9] nt
	s_add_u32 s8, s8, 0x1000
	s_addc_u32 s9, s9, 0
	global_store_dword v15, v26, s[8:9] nt
	s_add_u32 s8, s8, 0x1000
	s_addc_u32 s9, s9, 0
	global_store_dword v15, v27, s[8:9] nt
	s_add_u32 s8, s8, 0x5000
	s_addc_u32 s9, s9, 0
	global_store_dword v15, v28, s[8:9] nt
	s_add_u32 s8, s8, 0x1000
	s_addc_u32 s9, s9, 0
	global_store_dword v15, v29, s[8:9] nt
	s_add_u32 s8, s8, 0x1000
	s_addc_u32 s9, s9, 0
	global_store_dword v15, v30, s[8:9] nt
	s_add_u32 s8, s8, 0x1000
	s_addc_u32 s9, s9, 0
	global_store_dword v15, v31, s[8:9] nt
	s_add_u32 s8, s8, 0x5000
	s_addc_u32 s9, s9, 0
	global_store_dword v15, v32, s[8:9] nt
	s_add_u32 s8, s8, 0x1000
	s_addc_u32 s9, s9, 0
	global_store_dword v15, v33, s[8:9] nt
	s_add_u32 s8, s8, 0x1000
	s_addc_u32 s9, s9, 0
	global_store_dword v15, v34, s[8:9] nt
	s_add_u32 s8, s8, 0x1000
	s_addc_u32 s9, s9, 0
	global_store_dword v15, v35, s[8:9] nt
	s_add_u32 s8, s8, 0x5000
	s_addc_u32 s9, s9, 0
	global_store_dword v15, v36, s[8:9] nt
	s_add_u32 s8, s8, 0x1000
	s_addc_u32 s9, s9, 0
	global_store_dword v15, v37, s[8:9] nt
	s_add_u32 s8, s8, 0x1000
	s_addc_u32 s9, s9, 0
	global_store_dword v15, v38, s[8:9] nt
	s_add_u32 s8, s8, 0x1000
	s_addc_u32 s9, s9, 0
	global_store_dword v15, v39, s[8:9] nt
	s_add_u32 s8, s8, 0x5000
	s_addc_u32 s9, s9, 0
	global_store_dword v15, v40, s[8:9] nt
	s_add_u32 s8, s8, 0x1000
	s_addc_u32 s9, s9, 0
	global_store_dword v15, v41, s[8:9] nt
	s_add_u32 s8, s8, 0x1000
	s_addc_u32 s9, s9, 0
	global_store_dword v15, v42, s[8:9] nt
	s_add_u32 s8, s8, 0x1000
	s_addc_u32 s9, s9, 0
	global_store_dword v15, v43, s[8:9] nt
	s_add_u32 s8, s8, 0x5000
	s_addc_u32 s9, s9, 0
	global_store_dword v15, v44, s[8:9] nt
	s_add_u32 s8, s8, 0x1000
	s_addc_u32 s9, s9, 0
	global_store_dword v15, v45, s[8:9] nt
	s_add_u32 s8, s8, 0x1000
	s_addc_u32 s9, s9, 0
	global_store_dword v15, v46, s[8:9] nt
	s_add_u32 s8, s8, 0x1000
	s_addc_u32 s9, s9, 0
	global_store_dword v15, v47, s[8:9] nt
	s_endpgm
